# i4 + GEMM-phase prologue de-serialisation: the six stage-1 tile loads of every gemm_phase prologue are issued before the first counted wait (vmcnt(2) -> vmcnt(8)) so both prologue batches are in fligh
# baseline (speedup 1.0000x reference)
.LBB0_188:
	s_add_u32 s8, s52, 0x37600000
	s_addc_u32 s9, s53, 0
	s_lshl_b32 s10, s10, 5
	v_and_b32_e32 v17, 48, v1
	v_lshlrev_b32_e32 v18, 6, v1
	s_movk_i32 s0, 0x3c0
	v_lshlrev_b32_e32 v1, 2, v1
	s_and_b32 s39, s10, 0x60
	s_add_i32 m0, s34, 0x18000
	v_lshl_add_u64 v[10:11], v[10:11], 0, s[94:95]
	s_lshl_b32 s38, s11, 6
	s_lshl_b32 s11, s11, 13
	v_and_or_b32 v17, v18, s0, v17
	v_and_b32_e32 v1, 32, v1
	s_lshl_b32 s10, s39, 7
	global_load_lds_dwordx4 v[10:11], off
	v_lshl_add_u64 v[8:9], v[8:9], 0, s[94:95]
	s_add_i32 m0, s34, 0x1a000
	s_add_i32 s40, s34, 0x8000
	s_add_i32 s41, s34, 0xa000
	v_bitop3_b32 v18, v17, s11, v1 bitop3:0xde
	v_bitop3_b32 v1, s10, v17, v1 bitop3:0xf6
	global_load_lds_dwordx4 v[8:9], off
	v_lshl_add_u64 v[4:5], v[4:5], 0, s[94:95]
	s_mov_b32 m0, s40
	s_add_u32 s10, s20, 0x80080
	global_load_lds_dwordx4 v[4:5], off
	v_lshl_add_u64 v[4:5], v[6:7], 0, s[94:95]
	s_mov_b32 m0, s41
	s_addc_u32 s11, s21, 0
	global_load_lds_dwordx4 v[4:5], off
	s_add_i32 m0, s34, 0x1c000
	v_lshl_add_u64 v[4:5], s[10:11], 0, v[134:135]
	global_load_lds_dwordx4 v[4:5], off
	v_lshl_add_u64 v[4:5], s[10:11], 0, v[138:139]
	s_add_i32 m0, s34, 0x1e000
	s_cmpk_lt_u32 s3, 0x100
	global_load_lds_dwordx4 v[4:5], off
	s_waitcnt vmcnt(8)
	s_barrier
	v_lshlrev_b32_e32 v4, 15, v14
	v_and_b32_e32 v4, 0xffff0000, v4
	v_lshl_add_u32 v4, v15, 12, v4
	v_and_b32_e32 v5, 1, v14
	v_lshl_or_b32 v4, v5, 6, v4
	v_lshl_add_u32 v142, v16, 1, v4
	v_lshlrev_b32_e32 v4, 15, v2
	v_and_b32_e32 v4, 0xffff0000, v4
	s_waitcnt vmcnt(6)
	v_lshl_add_u32 v4, v12, 12, v4
	v_and_b32_e32 v2, 1, v2
	v_lshl_or_b32 v2, v2, 6, v4
	s_cselect_b64 s[10:11], -1, 0
	s_ashr_i32 s42, s25, 31
	v_mov_b32_e32 v143, v3
	v_lshl_add_u32 v144, v13, 1, v2
	v_mov_b32_e32 v145, v3
	s_mov_b32 s43, 0
	v_add_u32_e32 v133, 0, v18
	s_mov_b64 s[14:15], s[18:19]
	s_mov_b64 s[16:17], s[20:21]
	s_barrier
	s_waitcnt vmcnt(0)
	s_branch .LBB0_191

.LBB0_226:
	s_add_u32 s8, s52, 0x37a00000
	s_addc_u32 s9, s53, 0
	s_lshl_b32 s10, s10, 5
	v_and_b32_e32 v17, 48, v1
	v_lshlrev_b32_e32 v18, 6, v1
	s_movk_i32 s0, 0x3c0
	v_lshlrev_b32_e32 v1, 2, v1
	s_and_b32 s40, s10, 0x60
	s_add_i32 m0, s35, 0x18000
	v_lshl_add_u64 v[10:11], v[10:11], 0, s[94:95]
	s_lshl_b32 s39, s11, 6
	s_lshl_b32 s11, s11, 13
	v_and_or_b32 v17, v18, s0, v17
	v_and_b32_e32 v1, 32, v1
	s_lshl_b32 s10, s40, 7
	global_load_lds_dwordx4 v[10:11], off
	v_lshl_add_u64 v[8:9], v[8:9], 0, s[94:95]
	s_add_i32 m0, s35, 0x1a000
	s_add_i32 s41, s35, 0x8000
	s_add_i32 s42, s35, 0xa000
	v_bitop3_b32 v18, v17, s11, v1 bitop3:0xde
	v_bitop3_b32 v1, s10, v17, v1 bitop3:0xf6
	global_load_lds_dwordx4 v[8:9], off
	v_lshl_add_u64 v[4:5], v[4:5], 0, s[94:95]
	s_mov_b32 m0, s41
	s_add_u32 s10, s20, 0x80080
	global_load_lds_dwordx4 v[4:5], off
	v_lshl_add_u64 v[4:5], v[6:7], 0, s[94:95]
	s_mov_b32 m0, s42
	s_addc_u32 s11, s21, 0
	global_load_lds_dwordx4 v[4:5], off
	s_add_i32 m0, s35, 0x1c000
	v_lshl_add_u64 v[4:5], s[10:11], 0, v[134:135]
	global_load_lds_dwordx4 v[4:5], off
	v_lshl_add_u64 v[4:5], s[10:11], 0, v[138:139]
	s_add_i32 m0, s35, 0x1e000
	s_cmpk_lt_u32 s3, 0x100
	global_load_lds_dwordx4 v[4:5], off
	s_waitcnt vmcnt(8)
	s_barrier
	v_lshlrev_b32_e32 v4, 15, v14
	v_and_b32_e32 v4, 0xffff0000, v4
	v_lshl_add_u32 v4, v15, 12, v4
	v_and_b32_e32 v5, 1, v14
	v_lshl_or_b32 v4, v5, 6, v4
	v_lshl_add_u32 v142, v16, 1, v4
	v_lshlrev_b32_e32 v4, 15, v2
	v_and_b32_e32 v4, 0xffff0000, v4
	s_waitcnt vmcnt(6)
	v_lshl_add_u32 v4, v12, 12, v4
	v_and_b32_e32 v2, 1, v2
	v_lshl_or_b32 v2, v2, 6, v4
	s_cselect_b64 s[10:11], -1, 0
	s_ashr_i32 s43, s25, 31
	v_mov_b32_e32 v143, v3
	v_lshl_add_u32 v144, v13, 1, v2
	v_mov_b32_e32 v145, v3
	s_mov_b32 s44, 0
	v_add_u32_e32 v133, 0, v18
	s_mov_b64 s[14:15], s[18:19]
	s_mov_b64 s[16:17], s[20:21]
	s_barrier
	s_waitcnt vmcnt(0)
	s_branch .LBB0_229

.LBB0_718:
	s_add_u32 s4, s52, 0x3de00000
	s_addc_u32 s5, s53, 0
	s_lshl_b32 s2, s2, 5
	s_and_b32 s35, s2, 0x60
	s_add_i32 m0, s28, 0x18000
	v_lshl_add_u64 v[10:11], v[10:11], 0, s[94:95]
	s_lshl_b32 s34, s3, 6
	s_lshl_b32 s10, s3, 13
	s_lshl_b32 s11, s35, 7
	global_load_lds_dwordx4 v[10:11], off
	v_lshl_add_u64 v[8:9], v[8:9], 0, s[94:95]
	s_add_i32 m0, s28, 0x1a000
	s_add_i32 s36, s28, 0x8000
	s_add_i32 s37, s28, 0xa000
	global_load_lds_dwordx4 v[8:9], off
	v_lshl_add_u64 v[4:5], v[4:5], 0, s[94:95]
	s_mov_b32 m0, s36
	s_add_u32 s2, s18, 0x80080
	global_load_lds_dwordx4 v[4:5], off
	v_lshl_add_u64 v[4:5], v[6:7], 0, s[94:95]
	s_mov_b32 m0, s37
	s_addc_u32 s3, s19, 0
	global_load_lds_dwordx4 v[4:5], off
	s_add_i32 m0, s28, 0x1c000
	v_lshl_add_u64 v[4:5], s[2:3], 0, v[132:133]
	global_load_lds_dwordx4 v[4:5], off
	v_lshl_add_u64 v[4:5], s[2:3], 0, v[136:137]
	s_add_i32 m0, s28, 0x1e000
	s_movk_i32 s2, 0x3c0
	global_load_lds_dwordx4 v[4:5], off
	s_waitcnt vmcnt(8)
	s_barrier
	v_and_b32_e32 v4, 48, v1
	v_lshlrev_b32_e32 v5, 6, v1
	v_lshlrev_b32_e32 v1, 2, v1
	v_and_or_b32 v4, v5, s2, v4
	v_and_b32_e32 v1, 32, v1
	v_bitop3_b32 v5, v4, s10, v1 bitop3:0xde
	v_bitop3_b32 v1, s11, v4, v1 bitop3:0xf6
	v_lshlrev_b32_e32 v4, 15, v14
	v_and_b32_e32 v4, 0xffff0000, v4
	v_lshl_add_u32 v4, v15, 12, v4
	v_and_b32_e32 v6, 1, v14
	v_lshl_or_b32 v4, v6, 6, v4
	v_lshl_add_u32 v140, v16, 1, v4
	v_lshlrev_b32_e32 v4, 15, v2
	v_and_b32_e32 v4, 0xffff0000, v4
	s_waitcnt vmcnt(6)
	v_lshl_add_u32 v4, v12, 12, v4
	v_and_b32_e32 v2, 1, v2
	s_cmpk_lt_u32 s7, 0x100
	v_lshl_or_b32 v2, v2, 6, v4
	s_cselect_b64 s[10:11], -1, 0
	s_ashr_i32 s38, s92, 31
	v_mov_b32_e32 v141, v3
	v_lshl_add_u32 v142, v13, 1, v2
	v_mov_b32_e32 v143, v3
	s_mov_b32 s39, 0
	v_add_u32_e32 v144, 0, v5
	s_mov_b64 s[14:15], s[18:19]
	s_mov_b64 s[12:13], s[16:17]
	s_barrier
	s_branch .LBB0_721

.LBB0_899:
	s_add_u32 s8, s2, 0x42e00000
	v_readlane_b32 s52, v243, 8
	s_addc_u32 s9, s3, 0
	v_readlane_b32 s53, v243, 9
	s_cmp_eq_u32 s10, 0
	s_mov_b64 s[44:45], s[52:53]
	s_cselect_b32 s11, s45, 0
	s_cselect_b32 s10, s44, 0
	s_add_u32 s12, s2, 0x3be00000
	s_addc_u32 s13, s3, 0
	v_and_b32_e32 v17, 48, v1
	v_lshlrev_b32_e32 v18, 6, v1
	s_movk_i32 s3, 0x3c0
	v_lshlrev_b32_e32 v1, 2, v1
	s_lshl_b32 s2, s16, 13
	v_and_or_b32 v17, v18, s3, v17
	v_and_b32_e32 v1, 32, v1
	v_bitop3_b32 v18, v17, s2, v1 bitop3:0xde
	s_lshl_b32 s2, s15, 5
	s_and_b32 s41, s2, 0x60
	s_add_i32 m0, s35, 0x18000
	v_lshl_add_u64 v[10:11], v[10:11], 0, s[94:95]
	s_lshl_b32 s40, s16, 6
	s_lshl_b32 s2, s41, 7
	global_load_lds_dwordx4 v[10:11], off
	v_lshl_add_u64 v[8:9], v[8:9], 0, s[94:95]
	s_add_i32 m0, s35, 0x1a000
	s_add_i32 s42, s35, 0x8000
	s_add_i32 s43, s35, 0xa000
	v_bitop3_b32 v1, s2, v17, v1 bitop3:0xf6
	global_load_lds_dwordx4 v[8:9], off
	v_lshl_add_u64 v[4:5], v[4:5], 0, s[94:95]
	s_mov_b32 m0, s42
	s_add_u32 s2, s22, 0x80080
	global_load_lds_dwordx4 v[4:5], off
	v_lshl_add_u64 v[4:5], v[6:7], 0, s[94:95]
	s_mov_b32 m0, s43
	s_addc_u32 s3, s23, 0
	global_load_lds_dwordx4 v[4:5], off
	s_add_i32 m0, s35, 0x1c000
	v_lshl_add_u64 v[4:5], s[2:3], 0, v[140:141]
	global_load_lds_dwordx4 v[4:5], off
	v_lshl_add_u64 v[4:5], s[2:3], 0, v[144:145]
	s_add_i32 m0, s35, 0x1e000
	s_cmpk_lt_u32 s14, 0x100
	global_load_lds_dwordx4 v[4:5], off
	s_waitcnt vmcnt(8)
	s_barrier
	v_lshlrev_b32_e32 v4, 15, v14
	v_and_b32_e32 v4, 0xffff0000, v4
	v_lshl_add_u32 v4, v15, 12, v4
	v_and_b32_e32 v5, 1, v14
	v_lshl_or_b32 v4, v5, 6, v4
	v_lshl_add_u32 v148, v16, 1, v4
	v_lshlrev_b32_e32 v4, 15, v2
	v_and_b32_e32 v4, 0xffff0000, v4
	s_waitcnt vmcnt(6)
	s_cselect_b64 s[14:15], -1, 0
	s_ashr_i32 s44, s27, 31
	v_lshl_add_u32 v4, v12, 12, v4
	v_and_b32_e32 v2, 1, v2
	s_cmp_lg_u64 s[10:11], 0
	v_lshl_or_b32 v2, v2, 6, v4
	s_mov_b32 s39, 0
	s_cselect_b64 s[16:17], -1, 0
	v_mov_b32_e32 v149, v3
	v_lshl_add_u32 v150, v13, 1, v2
	v_mov_b32_e32 v151, v3
	v_add_u32_e32 v162, 0, v18
	s_mov_b64 s[18:19], s[4:5]
	s_mov_b64 s[20:21], s[22:23]
	v_readlane_b32 s54, v243, 10
	v_readlane_b32 s55, v243, 11
	v_readlane_b32 s56, v243, 12
	v_readlane_b32 s57, v243, 13
	v_readlane_b32 s58, v243, 14
	v_readlane_b32 s59, v243, 15
	v_readlane_b32 s60, v243, 16
	v_readlane_b32 s61, v243, 17
	v_readlane_b32 s62, v243, 18
	v_readlane_b32 s63, v243, 19
	v_readlane_b32 s64, v243, 20
	v_readlane_b32 s65, v243, 21
	v_readlane_b32 s66, v243, 22
	v_readlane_b32 s67, v243, 23
	s_barrier
	s_branch .LBB0_902

.LBB0_2108:
	s_add_u32 s4, s78, 0x4cf00000
	s_addc_u32 s5, s79, 0
	s_lshl_b32 s10, s10, 5
	s_waitcnt vmcnt(0)
	v_and_b32_e32 v12, 48, v1
	v_lshlrev_b32_e32 v13, 6, v1
	s_movk_i32 s12, 0x3c0
	v_lshlrev_b32_e32 v1, 2, v1
	s_and_b32 s37, s10, 0x60
	s_add_i32 m0, s26, 0x18000
	v_lshl_add_u64 v[10:11], v[10:11], 0, s[94:95]
	s_lshl_b32 s36, s11, 6
	s_lshl_b32 s11, s11, 13
	v_and_or_b32 v12, v13, s12, v12
	v_and_b32_e32 v1, 32, v1
	s_lshl_b32 s10, s37, 7
	global_load_lds_dwordx4 v[10:11], off
	v_lshl_add_u64 v[8:9], v[8:9], 0, s[94:95]
	s_add_i32 m0, s26, 0x1a000
	s_add_i32 s38, s26, 0x8000
	s_add_i32 s39, s26, 0xa000
	v_bitop3_b32 v13, v12, s11, v1 bitop3:0xde
	v_bitop3_b32 v1, s10, v12, v1 bitop3:0xf6
	global_load_lds_dwordx4 v[8:9], off
	v_lshl_add_u64 v[4:5], v[4:5], 0, s[94:95]
	s_mov_b32 m0, s38
	s_add_u32 s10, s16, 0x80080
	global_load_lds_dwordx4 v[4:5], off
	v_lshl_add_u64 v[4:5], v[6:7], 0, s[94:95]
	s_mov_b32 m0, s39
	s_addc_u32 s11, s17, 0
	global_load_lds_dwordx4 v[4:5], off
	s_add_i32 m0, s26, 0x1c000
	v_lshl_add_u64 v[4:5], s[10:11], 0, v[204:205]
	global_load_lds_dwordx4 v[4:5], off
	v_lshl_add_u64 v[4:5], s[10:11], 0, v[206:207]
	s_add_i32 m0, s26, 0x1e000
	s_cmpk_lt_u32 s7, 0x100
	global_load_lds_dwordx4 v[4:5], off
	s_waitcnt vmcnt(8)
	s_barrier
	s_waitcnt vmcnt(6)
	s_cselect_b64 s[10:11], -1, 0
	s_mov_b32 s41, 0
	v_add_u32_e32 v226, 0, v13
	s_barrier
	s_branch .LBB0_2111

.LBB0_2666:
	s_add_u32 s6, s74, 0x4fb00000
	s_addc_u32 s7, s75, 0
	s_add_u32 s4, s74, 0x37e00000
	s_addc_u32 s5, s75, 0
	v_and_b32_e32 v2, 48, v1
	v_lshlrev_b32_e32 v12, 6, v1
	s_movk_i32 s13, 0x3c0
	v_lshlrev_b32_e32 v1, 2, v1
	s_lshl_b32 s8, s8, 5
	s_lshl_b32 s58, s12, 6
	s_lshl_b32 s12, s12, 13
	v_and_or_b32 v2, v12, s13, v2
	v_and_b32_e32 v1, 32, v1
	s_and_b32 s8, s8, 0x60
	s_add_i32 m0, s54, 0x18000
	v_lshl_add_u64 v[10:11], v[10:11], 0, s[94:95]
	v_bitop3_b32 v12, v2, s12, v1 bitop3:0xde
	s_lshl_b32 s12, s8, 7
	global_load_lds_dwordx4 v[10:11], off
	v_lshl_add_u64 v[8:9], v[8:9], 0, s[94:95]
	s_add_i32 m0, s54, 0x1a000
	s_add_i32 s59, s54, 0x8000
	s_add_i32 s60, s54, 0xa000
	v_bitop3_b32 v1, s12, v2, v1 bitop3:0xf6
	global_load_lds_dwordx4 v[8:9], off
	v_lshl_add_u64 v[4:5], v[4:5], 0, s[94:95]
	s_mov_b32 m0, s59
	s_add_u32 s12, s28, 0x10080
	global_load_lds_dwordx4 v[4:5], off
	v_lshl_add_u64 v[4:5], v[6:7], 0, s[94:95]
	s_mov_b32 m0, s60
	s_addc_u32 s13, s29, 0
	global_load_lds_dwordx4 v[4:5], off
	s_add_i32 m0, s54, 0x1c000
	v_lshl_add_u64 v[4:5], s[12:13], 0, v[136:137]
	global_load_lds_dwordx4 v[4:5], off
	v_lshl_add_u64 v[4:5], s[12:13], 0, v[140:141]
	s_add_i32 m0, s54, 0x1e000
	s_cmpk_lt_u32 s9, 0x100
	global_load_lds_dwordx4 v[4:5], off
	s_waitcnt vmcnt(8)
	s_barrier
	s_waitcnt vmcnt(6)
	s_cselect_b64 s[12:13], -1, 0
	s_mov_b32 s9, s47
	s_mov_b32 s61, 0
	v_add_u32_e32 v146, 0, v12
	s_mov_b32 s74, 0x41800000
	s_barrier
	s_branch .LBB0_2669
